# baseline (speedup 1.0000x reference)
_Z9ssim_mainPKfS0_S0_Pf:
	v_readfirstlane_b32 s29, v0
	v_cmp_gt_u32_e32 vcc, 32, v0
	s_nop 1
	s_and_saveexec_b64 s[30:31], vcc
	v_mov_b32_e32 v1, 0x10000
	v_lshl_or_b32 v1, v0, 2, v1
	v_mov_b32_e32 v2, 0
	ds_write_b32 v1, v2
	s_or_b64 exec, exec, s[30:31]
	s_load_dwordx4 s[4:7], s[0:1], 0x0
	s_load_dwordx4 s[8:11], s[0:1], 0x10
	s_lshr_b32 s12, s29, 6
	s_mov_b32 s51, 0x44800000
	s_mov_b32 s38, 0
	s_mov_b32 s39, -1
	s_mov_b32 s92, -1
	s_mov_b32 s93, 0xffff
	s_mov_b32 s94, 0xffff
	s_mov_b32 s95, 0xffff
	v_and_b32_e32 v8, 63, v0
	v_and_b32_e32 v169, 15, v0
	v_bfe_u32 v164, v0, 4, 2
	v_lshlrev_b32_e32 v167, 3, v164
	v_xor_b32_e32 v168, 16, v167
	v_sub_u32_e32 v165, v167, v169
	v_sub_u32_e32 v166, v168, v169
	v_add_u32_e32 v172, 0, v165
	v_med3_i32 v172, v172, 0, 10
	v_lshlrev_b32_e32 v172, 2, v172
	v_add_u32_e32 v173, 1, v165
	v_med3_i32 v173, v173, 0, 10
	v_lshlrev_b32_e32 v173, 2, v173
	v_add_u32_e32 v174, 2, v165
	v_med3_i32 v174, v174, 0, 10
	v_lshlrev_b32_e32 v174, 2, v174
	v_add_u32_e32 v175, 3, v165
	v_med3_i32 v175, v175, 0, 10
	v_lshlrev_b32_e32 v175, 2, v175
	v_add_u32_e32 v176, 4, v165
	v_med3_i32 v176, v176, 0, 10
	v_lshlrev_b32_e32 v176, 2, v176
	v_add_u32_e32 v177, 5, v165
	v_med3_i32 v177, v177, 0, 10
	v_lshlrev_b32_e32 v177, 2, v177
	v_add_u32_e32 v178, 6, v165
	v_med3_i32 v178, v178, 0, 10
	v_lshlrev_b32_e32 v178, 2, v178
	v_add_u32_e32 v179, 7, v165
	v_med3_i32 v179, v179, 0, 10
	v_lshlrev_b32_e32 v179, 2, v179
	v_add_u32_e32 v180, 0, v166
	v_med3_i32 v180, v180, 0, 10
	v_lshlrev_b32_e32 v180, 2, v180
	v_add_u32_e32 v181, 1, v166
	v_med3_i32 v181, v181, 0, 10
	v_lshlrev_b32_e32 v181, 2, v181
	v_add_u32_e32 v182, 2, v166
	v_med3_i32 v182, v182, 0, 10
	v_lshlrev_b32_e32 v182, 2, v182
	v_add_u32_e32 v183, 3, v166
	v_med3_i32 v183, v183, 0, 10
	v_lshlrev_b32_e32 v183, 2, v183
	v_add_u32_e32 v184, 4, v166
	v_med3_i32 v184, v184, 0, 10
	v_lshlrev_b32_e32 v184, 2, v184
	v_add_u32_e32 v185, 5, v166
	v_med3_i32 v185, v185, 0, 10
	v_lshlrev_b32_e32 v185, 2, v185
	v_add_u32_e32 v186, 6, v166
	v_med3_i32 v186, v186, 0, 10
	v_lshlrev_b32_e32 v186, 2, v186
	v_add_u32_e32 v187, 7, v166
	v_med3_i32 v187, v187, 0, 10
	v_lshlrev_b32_e32 v187, 2, v187
	s_waitcnt lgkmcnt(0)
	global_load_dword v188, v172, s[8:9]
	global_load_dword v189, v173, s[8:9]
	global_load_dword v190, v174, s[8:9]
	global_load_dword v191, v175, s[8:9]
	global_load_dword v192, v176, s[8:9]
	global_load_dword v193, v177, s[8:9]
	global_load_dword v194, v178, s[8:9]
	global_load_dword v195, v179, s[8:9]
	global_load_dword v196, v180, s[8:9]
	global_load_dword v197, v181, s[8:9]
	global_load_dword v198, v182, s[8:9]
	global_load_dword v199, v183, s[8:9]
	global_load_dword v200, v184, s[8:9]
	global_load_dword v201, v185, s[8:9]
	global_load_dword v202, v186, s[8:9]
	global_load_dword v203, v187, s[8:9]
	s_load_dwordx8 s[40:47], s[8:9], 0x0
	s_load_dwordx2 s[48:49], s[8:9], 0x20
	s_load_dword s50, s[8:9], 0x28
	s_and_b32 s13, s2, 7
	s_lshl_b32 s13, s13, 5
	s_lshr_b32 s14, s2, 3
	s_add_u32 s13, s13, s14
	s_lshr_b32 s14, s13, 3
	s_and_b32 s15, s13, 7
	s_lshl_b32 s16, s14, 20
	s_lshl_b32 s17, s15, 17
	s_add_u32 s16, s16, s17
	s_lshl_b32 s17, s12, 8
	s_add_u32 s16, s16, s17
	s_add_u32 s18, s4, s16
	s_addc_u32 s19, s5, 0
	s_add_u32 s20, s6, s16
	s_addc_u32 s21, s7, 0
	s_mov_b32 s52, s18
	s_mov_b32 s53, s19
	s_add_u32 s54, s18, 0x1000
	s_addc_u32 s55, s19, 0
	s_add_u32 s56, s18, 0x2000
	s_addc_u32 s57, s19, 0
	s_add_u32 s58, s18, 0x3000
	s_addc_u32 s59, s19, 0
	s_add_u32 s60, s18, 0x10000
	s_addc_u32 s61, s19, 0
	s_add_u32 s62, s18, 0x11000
	s_addc_u32 s63, s19, 0
	s_add_u32 s64, s18, 0x12000
	s_addc_u32 s65, s19, 0
	s_add_u32 s66, s18, 0x13000
	s_addc_u32 s67, s19, 0
	s_mov_b32 s68, s20
	s_mov_b32 s69, s21
	s_add_u32 s70, s20, 0x1000
	s_addc_u32 s71, s21, 0
	s_add_u32 s72, s20, 0x2000
	s_addc_u32 s73, s21, 0
	s_add_u32 s74, s20, 0x3000
	s_addc_u32 s75, s21, 0
	s_add_u32 s76, s20, 0x10000
	s_addc_u32 s77, s21, 0
	s_add_u32 s78, s20, 0x11000
	s_addc_u32 s79, s21, 0
	s_add_u32 s80, s20, 0x12000
	s_addc_u32 s81, s21, 0
	s_add_u32 s82, s20, 0x13000
	s_addc_u32 s83, s21, 0
	s_cmp_eq_u32 s15, 7
	s_cselect_b32 s22, 0, 0x20000
	s_add_u32 s84, s18, s22
	s_addc_u32 s85, s19, 0
	s_add_u32 s86, s18, s22
	s_addc_u32 s87, s19, 0
	s_add_u32 s86, s86, 0x1000
	s_addc_u32 s87, s87, 0
	s_add_u32 s88, s20, s22
	s_addc_u32 s89, s21, 0
	s_add_u32 s90, s20, s22
	s_addc_u32 s91, s21, 0
	s_add_u32 s90, s90, 0x1000
	s_addc_u32 s91, s91, 0
	v_lshrrev_b32_e32 v167, 2, v169
	v_lshlrev_b32_e32 v167, 5, v167
	v_and_b32_e32 v168, 1, v169
	v_lshl_or_b32 v167, v168, 4, v167
	v_bfe_u32 v168, v169, 1, 1
	v_lshl_or_b32 v167, v168, 7, v167
	v_lshl_or_b32 v9, v164, 14, v167
	v_and_b32_e32 v168, 1, v164
	v_lshl_or_b32 v23, v168, 14, v167
	v_lshrrev_b32_e32 v168, 1, v164
	v_lshl_or_b32 v23, v168, 13, v23
	global_load_dwordx4 v[36:39], v9, s[52:53] offset:0 sc1 nt
	global_load_dwordx4 v[40:43], v9, s[52:53] offset:2048 sc1 nt
	global_load_dwordx4 v[68:71], v9, s[68:69] offset:0 sc1 nt
	global_load_dwordx4 v[72:75], v9, s[68:69] offset:2048 sc1 nt
	global_load_dwordx4 v[44:47], v9, s[54:55] offset:0 sc1 nt
	global_load_dwordx4 v[48:51], v9, s[54:55] offset:2048 sc1 nt
	global_load_dwordx4 v[76:79], v9, s[70:71] offset:0 sc1 nt
	global_load_dwordx4 v[80:83], v9, s[70:71] offset:2048 sc1 nt
	global_load_dwordx4 v[52:55], v9, s[56:57] offset:0 sc1 nt
	global_load_dwordx4 v[56:59], v9, s[56:57] offset:2048 sc1 nt
	global_load_dwordx4 v[84:87], v9, s[72:73] offset:0 sc1 nt
	global_load_dwordx4 v[88:91], v9, s[72:73] offset:2048 sc1 nt
	global_load_dwordx4 v[60:63], v9, s[58:59] offset:0 sc1 nt
	global_load_dwordx4 v[64:67], v9, s[58:59] offset:2048 sc1 nt
	global_load_dwordx4 v[92:95], v9, s[74:75] offset:0 sc1 nt
	global_load_dwordx4 v[96:99], v9, s[74:75] offset:2048 sc1 nt
	global_load_dwordx4 v[100:103], v9, s[60:61] offset:0 sc1 nt
	global_load_dwordx4 v[104:107], v9, s[60:61] offset:2048 sc1 nt
	global_load_dwordx4 v[132:135], v9, s[76:77] offset:0 sc1 nt
	global_load_dwordx4 v[136:139], v9, s[76:77] offset:2048 sc1 nt
	global_load_dwordx4 v[108:111], v9, s[62:63] offset:0 sc1 nt
	global_load_dwordx4 v[112:115], v9, s[62:63] offset:2048 sc1 nt
	global_load_dwordx4 v[140:143], v9, s[78:79] offset:0 sc1 nt
	global_load_dwordx4 v[144:147], v9, s[78:79] offset:2048 sc1 nt
	global_load_dwordx4 v[116:119], v9, s[64:65] offset:0 sc1 nt
	global_load_dwordx4 v[120:123], v9, s[64:65] offset:2048 sc1 nt
	global_load_dwordx4 v[148:151], v9, s[80:81] offset:0 sc1 nt
	global_load_dwordx4 v[152:155], v9, s[80:81] offset:2048 sc1 nt
	global_load_dwordx4 v[124:127], v9, s[66:67] offset:0 sc1 nt
	global_load_dwordx4 v[128:131], v9, s[66:67] offset:2048 sc1 nt
	global_load_dwordx4 v[156:159], v9, s[82:83] offset:0 sc1 nt
	global_load_dwordx4 v[160:163], v9, s[82:83] offset:2048 sc1 nt
	s_waitcnt lgkmcnt(0)
	v_mov_b32_e32 v229, 0x44800000
	v_fma_mixlo_f16 v228, s40, v229, 0
	v_cvt_f32_f16_e32 v228, v228
	v_cvt_f64_f32_e32 v[212:213], v228
	v_add_f64 v[212:213], v[212:213], 0
	v_fma_mixlo_f16 v228, s41, v229, 0
	v_cvt_f32_f16_e32 v228, v228
	v_cvt_f64_f32_e32 v[214:215], v228
	v_add_f64 v[212:213], v[212:213], v[214:215]
	v_fma_mixlo_f16 v228, s42, v229, 0
	v_cvt_f32_f16_e32 v228, v228
	v_cvt_f64_f32_e32 v[214:215], v228
	v_add_f64 v[212:213], v[212:213], v[214:215]
	v_fma_mixlo_f16 v228, s43, v229, 0
	v_cvt_f32_f16_e32 v228, v228
	v_cvt_f64_f32_e32 v[214:215], v228
	v_add_f64 v[212:213], v[212:213], v[214:215]
	v_fma_mixlo_f16 v228, s44, v229, 0
	v_cvt_f32_f16_e32 v228, v228
	v_cvt_f64_f32_e32 v[214:215], v228
	v_add_f64 v[212:213], v[212:213], v[214:215]
	v_fma_mixlo_f16 v228, s45, v229, 0
	v_cvt_f32_f16_e32 v228, v228
	v_cvt_f64_f32_e32 v[214:215], v228
	v_add_f64 v[212:213], v[212:213], v[214:215]
	v_fma_mixlo_f16 v228, s46, v229, 0
	v_cvt_f32_f16_e32 v228, v228
	v_cvt_f64_f32_e32 v[214:215], v228
	v_add_f64 v[212:213], v[212:213], v[214:215]
	v_fma_mixlo_f16 v228, s47, v229, 0
	v_cvt_f32_f16_e32 v228, v228
	v_cvt_f64_f32_e32 v[214:215], v228
	v_add_f64 v[212:213], v[212:213], v[214:215]
	v_fma_mixlo_f16 v228, s48, v229, 0
	v_cvt_f32_f16_e32 v228, v228
	v_cvt_f64_f32_e32 v[214:215], v228
	v_add_f64 v[212:213], v[212:213], v[214:215]
	v_fma_mixlo_f16 v228, s49, v229, 0
	v_cvt_f32_f16_e32 v228, v228
	v_cvt_f64_f32_e32 v[214:215], v228
	v_add_f64 v[212:213], v[212:213], v[214:215]
	v_fma_mixlo_f16 v228, s50, v229, 0
	v_cvt_f32_f16_e32 v228, v228
	v_cvt_f64_f32_e32 v[214:215], v228
	v_add_f64 v[212:213], v[212:213], v[214:215]
	v_mul_f64 v[212:213], v[212:213], v[212:213]
	v_mul_f64 v[216:217], v[212:213], 0.5
	v_add_f64 v[218:219], v[216:217], v[216:217]
	s_mov_b32 s36, 0xeb1c432d
	s_mov_b32 s37, 0x3f1a36e2
	v_mul_f64 v[220:221], v[212:213], s[36:37]
	v_mul_f64 v[222:223], v[216:217], v[218:219]
	v_fmac_f64_e32 v[222:223], v[212:213], v[220:221]
	v_add_f64 v[224:225], v[212:213], v[212:213]
	s_mov_b32 s36, 0x487fcb92
	s_mov_b32 s37, 0x3f4d7dbf
	v_mul_f64 v[226:227], v[212:213], s[36:37]
	v_cvt_f32_f64_e32 v0, v[226:227]
	v_mov_b32_e32 v1, v0
	v_mov_b32_e32 v2, v0
	v_mov_b32_e32 v3, v0
	v_cvt_f32_f64_e32 v10, v[218:219]
	v_cvt_f32_f64_e32 v11, v[222:223]
	v_cvt_f32_f64_e32 v12, v[212:213]
	v_cvt_f32_f64_e32 v13, v[224:225]
	v_mul_f64 v[226:227], v[212:213], v[226:227]
	v_cvt_f32_f64_e32 v14, v[226:227]
	v_lshlrev_b32_e32 v167, 2, v164
	s_cmp_eq_u32 s12, 0
	s_cselect_b32 s23, 6, 64
	v_add_u32_e32 v168, 0, v167
	v_cmp_gt_u32_e32 vcc, s23, v168
	s_nop 1
	v_cndmask_b32_e64 v15, 0, 1.0, vcc
	v_add_u32_e32 v168, 1, v167
	v_cmp_gt_u32_e32 vcc, s23, v168
	s_nop 1
	v_cndmask_b32_e64 v16, 0, 1.0, vcc
	v_add_u32_e32 v168, 2, v167
	v_cmp_gt_u32_e32 vcc, s23, v168
	s_nop 1
	v_cndmask_b32_e64 v17, 0, 1.0, vcc
	v_add_u32_e32 v168, 3, v167
	v_cmp_gt_u32_e32 vcc, s23, v168
	s_nop 1
	v_cndmask_b32_e64 v18, 0, 1.0, vcc
	v_and_b32_e32 v167, 31, v8
	v_lshlrev_b32_e32 v167, 4, v167
	s_lshl_b32 s24, s12, 11
	s_add_i32 s25, s12, 7
	s_and_b32 s25, s25, 7
	s_lshl_b32 s26, s25, 11
	v_or_b32_e32 v4, s24, v167
	v_or_b32_e32 v5, s26, v167
	s_lshl_b32 s27, s12, 2
	s_add_u32 s27, s27, 0x10000
	s_lshl_b32 s28, s25, 2
	s_add_u32 s28, s28, 0x10000
	v_mov_b32_e32 v6, s27
	v_mov_b32_e32 v7, s28
	v_mov_b32_e32 v19, 0
	v_mov_b32_e32 v20, 0
	v_mov_b32_e32 v21, 0
	v_mov_b32_e32 v22, 0
	s_waitcnt vmcnt(32)
	v_cmp_lt_u32_e64 s[32:33], 31, v8
	v_cmp_gt_u32_e64 s[34:35], 32, v8
	v_fma_mixlo_f16 v204, v188, s51, 0
	v_add_u32_e32 v167, 0, v165
	v_cmp_gt_u32_e32 vcc, 11, v167
	s_nop 1
	v_cndmask_b32_e32 v204, 0, v204, vcc
	v_fma_mixlo_f16 v205, v189, s51, 0
	v_add_u32_e32 v167, 1, v165
	v_cmp_gt_u32_e32 vcc, 11, v167
	s_nop 1
	v_cndmask_b32_e32 v205, 0, v205, vcc
	v_fma_mixlo_f16 v206, v190, s51, 0
	v_add_u32_e32 v167, 2, v165
	v_cmp_gt_u32_e32 vcc, 11, v167
	s_nop 1
	v_cndmask_b32_e32 v206, 0, v206, vcc
	v_fma_mixlo_f16 v207, v191, s51, 0
	v_add_u32_e32 v167, 3, v165
	v_cmp_gt_u32_e32 vcc, 11, v167
	s_nop 1
	v_cndmask_b32_e32 v207, 0, v207, vcc
	v_fma_mixlo_f16 v208, v192, s51, 0
	v_add_u32_e32 v167, 4, v165
	v_cmp_gt_u32_e32 vcc, 11, v167
	s_nop 1
	v_cndmask_b32_e32 v208, 0, v208, vcc
	v_fma_mixlo_f16 v209, v193, s51, 0
	v_add_u32_e32 v167, 5, v165
	v_cmp_gt_u32_e32 vcc, 11, v167
	s_nop 1
	v_cndmask_b32_e32 v209, 0, v209, vcc
	v_fma_mixlo_f16 v210, v194, s51, 0
	v_add_u32_e32 v167, 6, v165
	v_cmp_gt_u32_e32 vcc, 11, v167
	s_nop 1
	v_cndmask_b32_e32 v210, 0, v210, vcc
	v_fma_mixlo_f16 v211, v195, s51, 0
	v_add_u32_e32 v167, 7, v165
	v_cmp_gt_u32_e32 vcc, 11, v167
	s_nop 1
	v_cndmask_b32_e32 v211, 0, v211, vcc
	v_pack_b32_f16 v24, v204, v205
	v_pack_b32_f16 v25, v206, v207
	v_pack_b32_f16 v26, v208, v209
	v_pack_b32_f16 v27, v210, v211
	v_fma_mixlo_f16 v204, v196, s51, 0
	v_add_u32_e32 v167, 0, v166
	v_cmp_gt_u32_e32 vcc, 11, v167
	s_nop 1
	v_cndmask_b32_e32 v204, 0, v204, vcc
	v_fma_mixlo_f16 v205, v197, s51, 0
	v_add_u32_e32 v167, 1, v166
	v_cmp_gt_u32_e32 vcc, 11, v167
	s_nop 1
	v_cndmask_b32_e32 v205, 0, v205, vcc
	v_fma_mixlo_f16 v206, v198, s51, 0
	v_add_u32_e32 v167, 2, v166
	v_cmp_gt_u32_e32 vcc, 11, v167
	s_nop 1
	v_cndmask_b32_e32 v206, 0, v206, vcc
	v_fma_mixlo_f16 v207, v199, s51, 0
	v_add_u32_e32 v167, 3, v166
	v_cmp_gt_u32_e32 vcc, 11, v167
	s_nop 1
	v_cndmask_b32_e32 v207, 0, v207, vcc
	v_fma_mixlo_f16 v208, v200, s51, 0
	v_add_u32_e32 v167, 4, v166
	v_cmp_gt_u32_e32 vcc, 11, v167
	s_nop 1
	v_cndmask_b32_e32 v208, 0, v208, vcc
	v_fma_mixlo_f16 v209, v201, s51, 0
	v_add_u32_e32 v167, 5, v166
	v_cmp_gt_u32_e32 vcc, 11, v167
	s_nop 1
	v_cndmask_b32_e32 v209, 0, v209, vcc
	v_fma_mixlo_f16 v210, v202, s51, 0
	v_add_u32_e32 v167, 6, v166
	v_cmp_gt_u32_e32 vcc, 11, v167
	s_nop 1
	v_cndmask_b32_e32 v210, 0, v210, vcc
	v_fma_mixlo_f16 v211, v203, s51, 0
	v_add_u32_e32 v167, 7, v166
	v_cmp_gt_u32_e32 vcc, 11, v167
	s_nop 1
	v_cndmask_b32_e32 v211, 0, v211, vcc
	v_pack_b32_f16 v167, v204, v205
	v_cndmask_b32_e64 v28, 0, v167, s[32:33]
	v_cndmask_b32_e64 v32, 0, v167, s[34:35]
	v_pack_b32_f16 v167, v206, v207
	v_cndmask_b32_e64 v29, 0, v167, s[32:33]
	v_cndmask_b32_e64 v33, 0, v167, s[34:35]
	v_pack_b32_f16 v167, v208, v209
	v_cndmask_b32_e64 v30, 0, v167, s[32:33]
	v_cndmask_b32_e64 v34, 0, v167, s[34:35]
	v_pack_b32_f16 v167, v210, v211
	v_cndmask_b32_e64 v31, 0, v167, s[32:33]
	v_cndmask_b32_e64 v35, 0, v167, s[34:35]
	s_waitcnt lgkmcnt(0)
	s_barrier
	s_waitcnt vmcnt(28)
	v_cvt_pk_f16_f32 v164, v36, v40
	v_cvt_pk_f16_f32 v180, v68, v72
	v_pk_add_f16 v164, v164, -0.5 op_sel_hi:[1,0]
	v_pk_add_f16 v180, v180, -0.5 op_sel_hi:[1,0]
	v_pk_mul_f16 v196, v180, v180
	v_pk_mul_f16 v212, v164, v180
	v_pk_fma_f16 v196, v164, v164, v196
	v_cvt_pk_f16_f32 v168, v37, v41
	v_cvt_pk_f16_f32 v184, v69, v73
	v_pk_add_f16 v168, v168, -0.5 op_sel_hi:[1,0]
	v_pk_add_f16 v184, v184, -0.5 op_sel_hi:[1,0]
	v_pk_mul_f16 v200, v184, v184
	v_pk_mul_f16 v216, v168, v184
	v_pk_fma_f16 v200, v168, v168, v200
	v_cvt_pk_f16_f32 v172, v38, v42
	v_cvt_pk_f16_f32 v188, v70, v74
	v_pk_add_f16 v172, v172, -0.5 op_sel_hi:[1,0]
	v_pk_add_f16 v188, v188, -0.5 op_sel_hi:[1,0]
	v_pk_mul_f16 v204, v188, v188
	v_pk_mul_f16 v220, v172, v188
	v_pk_fma_f16 v204, v172, v172, v204
	v_cvt_pk_f16_f32 v176, v39, v43
	v_cvt_pk_f16_f32 v192, v71, v75
	v_pk_add_f16 v176, v176, -0.5 op_sel_hi:[1,0]
	v_pk_add_f16 v192, v192, -0.5 op_sel_hi:[1,0]
	v_pk_mul_f16 v208, v192, v192
	v_pk_mul_f16 v224, v176, v192
	v_pk_fma_f16 v208, v176, v176, v208
	s_waitcnt vmcnt(24)
	v_cvt_pk_f16_f32 v165, v44, v48
	v_cvt_pk_f16_f32 v181, v76, v80
	v_pk_add_f16 v165, v165, -0.5 op_sel_hi:[1,0]
	v_pk_add_f16 v181, v181, -0.5 op_sel_hi:[1,0]
	v_pk_mul_f16 v197, v181, v181
	v_pk_mul_f16 v213, v165, v181
	v_pk_fma_f16 v197, v165, v165, v197
	v_cvt_pk_f16_f32 v169, v45, v49
	v_cvt_pk_f16_f32 v185, v77, v81
	v_pk_add_f16 v169, v169, -0.5 op_sel_hi:[1,0]
	v_pk_add_f16 v185, v185, -0.5 op_sel_hi:[1,0]
	v_pk_mul_f16 v201, v185, v185
	v_pk_mul_f16 v217, v169, v185
	v_pk_fma_f16 v201, v169, v169, v201
	v_cvt_pk_f16_f32 v173, v46, v50
	v_cvt_pk_f16_f32 v189, v78, v82
	v_pk_add_f16 v173, v173, -0.5 op_sel_hi:[1,0]
	v_pk_add_f16 v189, v189, -0.5 op_sel_hi:[1,0]
	v_pk_mul_f16 v205, v189, v189
	v_pk_mul_f16 v221, v173, v189
	v_pk_fma_f16 v205, v173, v173, v205
	v_cvt_pk_f16_f32 v177, v47, v51
	v_cvt_pk_f16_f32 v193, v79, v83
	v_pk_add_f16 v177, v177, -0.5 op_sel_hi:[1,0]
	v_pk_add_f16 v193, v193, -0.5 op_sel_hi:[1,0]
	v_pk_mul_f16 v209, v193, v193
	v_pk_mul_f16 v225, v177, v193
	v_pk_fma_f16 v209, v177, v177, v209
	s_waitcnt vmcnt(20)
	v_cvt_pk_f16_f32 v166, v52, v56
	v_cvt_pk_f16_f32 v182, v84, v88
	v_pk_add_f16 v166, v166, -0.5 op_sel_hi:[1,0]
	v_pk_add_f16 v182, v182, -0.5 op_sel_hi:[1,0]
	v_pk_mul_f16 v198, v182, v182
	v_pk_mul_f16 v214, v166, v182
	v_pk_fma_f16 v198, v166, v166, v198
	v_cvt_pk_f16_f32 v170, v53, v57
	v_cvt_pk_f16_f32 v186, v85, v89
	v_pk_add_f16 v170, v170, -0.5 op_sel_hi:[1,0]
	v_pk_add_f16 v186, v186, -0.5 op_sel_hi:[1,0]
	v_pk_mul_f16 v202, v186, v186
	v_pk_mul_f16 v218, v170, v186
	v_pk_fma_f16 v202, v170, v170, v202
	v_cvt_pk_f16_f32 v174, v54, v58
	v_cvt_pk_f16_f32 v190, v86, v90
	v_pk_add_f16 v174, v174, -0.5 op_sel_hi:[1,0]
	v_pk_add_f16 v190, v190, -0.5 op_sel_hi:[1,0]
	v_pk_mul_f16 v206, v190, v190
	v_pk_mul_f16 v222, v174, v190
	v_pk_fma_f16 v206, v174, v174, v206
	v_cvt_pk_f16_f32 v178, v55, v59
	v_cvt_pk_f16_f32 v194, v87, v91
	v_pk_add_f16 v178, v178, -0.5 op_sel_hi:[1,0]
	v_pk_add_f16 v194, v194, -0.5 op_sel_hi:[1,0]
	v_pk_mul_f16 v210, v194, v194
	v_pk_mul_f16 v226, v178, v194
	v_pk_fma_f16 v210, v178, v178, v210
	s_waitcnt vmcnt(16)
	v_cvt_pk_f16_f32 v167, v60, v64
	v_cvt_pk_f16_f32 v183, v92, v96
	v_pk_add_f16 v167, v167, -0.5 op_sel_hi:[1,0]
	v_pk_add_f16 v183, v183, -0.5 op_sel_hi:[1,0]
	v_pk_mul_f16 v199, v183, v183
	v_pk_mul_f16 v215, v167, v183
	v_pk_fma_f16 v199, v167, v167, v199
	v_cvt_pk_f16_f32 v171, v61, v65
	v_cvt_pk_f16_f32 v187, v93, v97
	v_pk_add_f16 v171, v171, -0.5 op_sel_hi:[1,0]
	v_pk_add_f16 v187, v187, -0.5 op_sel_hi:[1,0]
	v_pk_mul_f16 v203, v187, v187
	v_pk_mul_f16 v219, v171, v187
	v_pk_fma_f16 v203, v171, v171, v203
	v_cvt_pk_f16_f32 v175, v62, v66
	v_cvt_pk_f16_f32 v191, v94, v98
	v_pk_add_f16 v175, v175, -0.5 op_sel_hi:[1,0]
	v_pk_add_f16 v191, v191, -0.5 op_sel_hi:[1,0]
	v_pk_mul_f16 v207, v191, v191
	v_pk_mul_f16 v223, v175, v191
	v_pk_fma_f16 v207, v175, v175, v207
	v_cvt_pk_f16_f32 v179, v63, v67
	v_cvt_pk_f16_f32 v195, v95, v99
	v_pk_add_f16 v179, v179, -0.5 op_sel_hi:[1,0]
	v_pk_add_f16 v195, v195, -0.5 op_sel_hi:[1,0]
	v_pk_mul_f16 v211, v195, v195
	v_pk_mul_f16 v227, v179, v195
	v_pk_fma_f16 v211, v179, v179, v211
	v_mfma_f32_16x16x32_f16 v[68:71], v[164:167], v[24:27], 0
	v_mfma_f32_16x16x32_f16 v[72:75], v[168:171], v[24:27], 0
	v_mfma_f32_16x16x32_f16 v[76:79], v[172:175], v[24:27], 0
	v_mfma_f32_16x16x32_f16 v[80:83], v[176:179], v[24:27], 0
	v_mfma_f32_16x16x32_f16 v[84:87], v[180:183], v[24:27], 0
	v_mfma_f32_16x16x32_f16 v[88:91], v[184:187], v[24:27], 0
	v_mfma_f32_16x16x32_f16 v[92:95], v[188:191], v[24:27], 0
	v_mfma_f32_16x16x32_f16 v[96:99], v[192:195], v[24:27], 0
	s_nop 1
	v_cvt_pk_f16_f32 v36, v68, v72
	s_nop 0
	v_cvt_pk_f16_f32 v37, v76, v80
	v_cvt_pk_f16_f32 v38, v69, v73
	v_cvt_pk_f16_f32 v39, v77, v81
	v_cvt_pk_f16_f32 v40, v70, v74
	v_cvt_pk_f16_f32 v41, v78, v82
	v_cvt_pk_f16_f32 v42, v71, v75
	v_cvt_pk_f16_f32 v43, v79, v83
	v_mfma_f32_16x16x32_f16 v[68:71], v[196:199], v[24:27], 0
	v_mfma_f32_16x16x32_f16 v[72:75], v[200:203], v[24:27], 0
	v_mfma_f32_16x16x32_f16 v[76:79], v[204:207], v[24:27], 0
	v_mfma_f32_16x16x32_f16 v[80:83], v[208:211], v[24:27], 0
	v_cvt_pk_f16_f32 v44, v84, v88
	v_cvt_pk_f16_f32 v45, v92, v96
	v_cvt_pk_f16_f32 v46, v85, v89
	v_cvt_pk_f16_f32 v47, v93, v97
	v_cvt_pk_f16_f32 v48, v86, v90
	v_cvt_pk_f16_f32 v49, v94, v98
	v_cvt_pk_f16_f32 v50, v87, v91
	v_cvt_pk_f16_f32 v51, v95, v99
	v_mfma_f32_16x16x32_f16 v[84:87], v[212:215], v[24:27], 0
	v_mfma_f32_16x16x32_f16 v[88:91], v[216:219], v[24:27], 0
	v_mfma_f32_16x16x32_f16 v[92:95], v[220:223], v[24:27], 0
	v_mfma_f32_16x16x32_f16 v[96:99], v[224:227], v[24:27], 0
	v_cvt_pk_f16_f32 v52, v68, v72
	v_cvt_pk_f16_f32 v53, v76, v80
	v_cvt_pk_f16_f32 v54, v69, v73
	v_cvt_pk_f16_f32 v55, v77, v81
	v_cvt_pk_f16_f32 v56, v70, v74
	v_cvt_pk_f16_f32 v57, v78, v82
	v_cvt_pk_f16_f32 v58, v71, v75
	v_cvt_pk_f16_f32 v59, v79, v83
	v_cvt_pk_f16_f32 v60, v84, v88
	v_cvt_pk_f16_f32 v61, v92, v96
	v_cvt_pk_f16_f32 v62, v85, v89
	v_cvt_pk_f16_f32 v63, v93, v97
	v_cvt_pk_f16_f32 v64, v86, v90
	v_cvt_pk_f16_f32 v65, v94, v98
	v_cvt_pk_f16_f32 v66, v87, v91
	v_cvt_pk_f16_f32 v67, v95, v99
	s_mov_b64 exec, s[38:39]
	ds_write_b128 v4, v[40:43] offset:0
	ds_write_b128 v4, v[48:51] offset:512
	ds_write_b128 v4, v[56:59] offset:1024
	ds_write_b128 v4, v[64:67] offset:1536
	s_mov_b64 exec, -1
	v_mfma_f32_16x16x32_f16 v[68:71], v[24:27], v[36:39], 0
	v_mfma_f32_16x16x32_f16 v[72:75], v[24:27], v[44:47], 0
	v_mfma_f32_16x16x32_f16 v[76:79], v[24:27], v[52:55], v[0:3]
	v_mfma_f32_16x16x32_f16 v[80:83], v[24:27], v[60:63], 0
	v_mfma_f32_16x16x32_f16 v[84:87], v[28:31], v[36:39], 0
	v_mfma_f32_16x16x32_f16 v[88:91], v[28:31], v[44:47], 0
	v_mfma_f32_16x16x32_f16 v[92:95], v[28:31], v[52:55], v[0:3]
	v_mfma_f32_16x16x32_f16 v[96:99], v[28:31], v[60:63], 0
	v_mfma_f32_16x16x32_f16 v[84:87], v[32:35], v[40:43], v[84:87]
	v_mfma_f32_16x16x32_f16 v[88:91], v[32:35], v[48:51], v[88:91]
	v_mfma_f32_16x16x32_f16 v[92:95], v[32:35], v[56:59], v[92:95]
	v_mfma_f32_16x16x32_f16 v[96:99], v[32:35], v[64:67], v[96:99]
	s_waitcnt lgkmcnt(0)
	ds_write_b32 v6, v6 offset:0
	ds_read_b32 v9, v7 offset:0
	v_mul_f32_e32 v244, v68, v72
	v_mul_f32_e32 v250, v69, v73
	v_mul_f32_e64 v245, -v72, v72
	v_mul_f32_e64 v251, -v73, v73
	v_add_f32_e32 v246, v68, v72
	v_add_f32_e32 v252, v69, v73
	v_fma_f32 v245, -v68, v68, v245
	v_fma_f32 v251, -v69, v69, v251
	v_fma_f32 v247, v10, v246, v11
	v_fma_f32 v253, v10, v252, v11
	v_fma_f32 v246, v13, v80, v14
	v_fma_f32 v252, v13, v81, v14
	v_fma_f32 v248, v12, v76, v245
	v_fma_f32 v254, v12, v77, v251
	v_fma_f32 v249, 2.0, v244, v247
	v_fma_f32 v255, 2.0, v250, v253
	v_sub_f32_e32 v247, v247, v245
	v_sub_f32_e32 v253, v253, v251
	v_fma_f32 v246, -2.0, v244, v246
	v_fma_f32 v252, -2.0, v250, v252
	v_mul_f32_e32 v247, v247, v248
	v_mul_f32_e32 v253, v253, v254
	v_rcp_f32_e32 v247, v247
	v_rcp_f32_e32 v253, v253
	v_mul_f32_e32 v249, v249, v246
	v_mul_f32_e32 v255, v255, v252
	v_fma_f32 v19, v249, v247, v19
	v_fma_f32 v19, v255, v253, v19
	v_mul_f32_e32 v244, v70, v74
	v_mul_f32_e32 v250, v71, v75
	v_mul_f32_e64 v245, -v74, v74
	v_mul_f32_e64 v251, -v75, v75
	v_add_f32_e32 v246, v70, v74
	v_add_f32_e32 v252, v71, v75
	v_fma_f32 v245, -v70, v70, v245
	v_fma_f32 v251, -v71, v71, v251
	v_fma_f32 v247, v10, v246, v11
	v_fma_f32 v253, v10, v252, v11
	v_fma_f32 v246, v13, v82, v14
	v_fma_f32 v252, v13, v83, v14
	v_fma_f32 v248, v12, v78, v245
	v_fma_f32 v254, v12, v79, v251
	v_fma_f32 v249, 2.0, v244, v247
	v_fma_f32 v255, 2.0, v250, v253
	v_sub_f32_e32 v247, v247, v245
	v_sub_f32_e32 v253, v253, v251
	v_fma_f32 v246, -2.0, v244, v246
	v_fma_f32 v252, -2.0, v250, v252
	v_mul_f32_e32 v247, v247, v248
	v_mul_f32_e32 v253, v253, v254
	v_rcp_f32_e32 v247, v247
	v_rcp_f32_e32 v253, v253
	v_mul_f32_e32 v249, v249, v246
	v_mul_f32_e32 v255, v255, v252
	v_fma_f32 v20, v249, v247, v20
	v_fma_f32 v20, v255, v253, v20
	v_mfma_f32_16x16x32_f16 v[68:71], v[24:27], v[40:43], 0
	v_mfma_f32_16x16x32_f16 v[72:75], v[24:27], v[48:51], 0
	v_mfma_f32_16x16x32_f16 v[76:79], v[24:27], v[56:59], v[0:3]
	v_mfma_f32_16x16x32_f16 v[80:83], v[24:27], v[64:67], 0
	s_waitcnt lgkmcnt(0)
	v_cmp_ne_u32_e32 vcc, 0, v9
	s_cbranch_vccnz .Lq_go_0

.Lq_go_0:
	ds_read_b128 v[228:231], v5 offset:0
	ds_read_b128 v[232:235], v5 offset:512
	ds_read_b128 v[236:239], v5 offset:1024
	ds_read_b128 v[240:243], v5 offset:1536
	v_mul_f32_e32 v244, v84, v88
	v_mul_f32_e32 v250, v85, v89
	v_mul_f32_e64 v245, -v88, v88
	v_mul_f32_e64 v251, -v89, v89
	v_add_f32_e32 v246, v84, v88
	v_add_f32_e32 v252, v85, v89
	v_fma_f32 v245, -v84, v84, v245
	v_fma_f32 v251, -v85, v85, v251
	v_fma_f32 v247, v10, v246, v11
	v_fma_f32 v253, v10, v252, v11
	v_fma_f32 v246, v13, v96, v14
	v_fma_f32 v252, v13, v97, v14
	v_fma_f32 v248, v12, v92, v245
	v_fma_f32 v254, v12, v93, v251
	v_fma_f32 v249, 2.0, v244, v247
	v_fma_f32 v255, 2.0, v250, v253
	v_sub_f32_e32 v247, v247, v245
	v_sub_f32_e32 v253, v253, v251
	v_fma_f32 v246, -2.0, v244, v246
	v_fma_f32 v252, -2.0, v250, v252
	v_mul_f32_e32 v247, v247, v248
	v_mul_f32_e32 v253, v253, v254
	v_rcp_f32_e32 v247, v247
	v_rcp_f32_e32 v253, v253
	v_mul_f32_e32 v249, v249, v246
	v_mul_f32_e32 v255, v255, v252
	v_fma_f32 v19, v249, v247, v19
	v_fma_f32 v19, v255, v253, v19
	v_mul_f32_e32 v244, v86, v90
	v_mul_f32_e32 v250, v87, v91
	v_mul_f32_e64 v245, -v90, v90
	v_mul_f32_e64 v251, -v91, v91
	v_add_f32_e32 v246, v86, v90
	v_add_f32_e32 v252, v87, v91
	v_fma_f32 v245, -v86, v86, v245
	v_fma_f32 v251, -v87, v87, v251
	v_fma_f32 v247, v10, v246, v11
	v_fma_f32 v253, v10, v252, v11
	v_fma_f32 v246, v13, v98, v14
	v_fma_f32 v252, v13, v99, v14
	v_fma_f32 v248, v12, v94, v245
	v_fma_f32 v254, v12, v95, v251
	v_fma_f32 v249, 2.0, v244, v247
	v_fma_f32 v255, 2.0, v250, v253
	v_sub_f32_e32 v247, v247, v245
	v_sub_f32_e32 v253, v253, v251
	v_fma_f32 v246, -2.0, v244, v246
	v_fma_f32 v252, -2.0, v250, v252
	v_mul_f32_e32 v247, v247, v248
	v_mul_f32_e32 v253, v253, v254
	v_rcp_f32_e32 v247, v247
	v_rcp_f32_e32 v253, v253
	v_mul_f32_e32 v249, v249, v246
	v_mul_f32_e32 v255, v255, v252
	v_fma_f32 v20, v249, v247, v20
	v_fma_f32 v20, v255, v253, v20
	s_waitcnt lgkmcnt(0)
	v_mfma_f32_16x16x32_f16 v[84:87], v[28:31], v[228:231], 0
	v_mfma_f32_16x16x32_f16 v[88:91], v[28:31], v[232:235], 0
	v_mfma_f32_16x16x32_f16 v[92:95], v[28:31], v[236:239], v[0:3]
	v_mfma_f32_16x16x32_f16 v[96:99], v[28:31], v[240:243], 0
	v_mfma_f32_16x16x32_f16 v[84:87], v[32:35], v[36:39], v[84:87]
	v_mfma_f32_16x16x32_f16 v[88:91], v[32:35], v[44:47], v[88:91]
	v_mfma_f32_16x16x32_f16 v[92:95], v[32:35], v[52:55], v[92:95]
	v_mfma_f32_16x16x32_f16 v[96:99], v[32:35], v[60:63], v[96:99]
	v_mul_f32_e32 v244, v68, v72
	v_mul_f32_e32 v250, v69, v73
	v_mul_f32_e64 v245, -v72, v72
	v_mul_f32_e64 v251, -v73, v73
	v_add_f32_e32 v246, v68, v72
	v_add_f32_e32 v252, v69, v73
	v_fma_f32 v245, -v68, v68, v245
	v_fma_f32 v251, -v69, v69, v251
	v_fma_f32 v247, v10, v246, v11
	v_fma_f32 v253, v10, v252, v11
	v_fma_f32 v246, v13, v80, v14
	v_fma_f32 v252, v13, v81, v14
	v_fma_f32 v248, v12, v76, v245
	v_fma_f32 v254, v12, v77, v251
	v_fma_f32 v249, 2.0, v244, v247
	v_fma_f32 v255, 2.0, v250, v253
	v_sub_f32_e32 v247, v247, v245
	v_sub_f32_e32 v253, v253, v251
	v_fma_f32 v246, -2.0, v244, v246
	v_fma_f32 v252, -2.0, v250, v252
	v_mul_f32_e32 v247, v247, v248
	v_mul_f32_e32 v253, v253, v254
	v_rcp_f32_e32 v247, v247
	v_rcp_f32_e32 v253, v253
	v_mul_f32_e32 v249, v249, v246
	v_mul_f32_e32 v255, v255, v252
	v_fma_f32 v19, v249, v247, v19
	v_fma_f32 v19, v255, v253, v19
	v_mul_f32_e32 v244, v70, v74
	v_mul_f32_e32 v250, v71, v75
	v_mul_f32_e64 v245, -v74, v74
	v_mul_f32_e64 v251, -v75, v75
	v_add_f32_e32 v246, v70, v74
	v_add_f32_e32 v252, v71, v75
	v_fma_f32 v245, -v70, v70, v245
	v_fma_f32 v251, -v71, v71, v251
	v_fma_f32 v247, v10, v246, v11
	v_fma_f32 v253, v10, v252, v11
	v_fma_f32 v246, v13, v82, v14
	v_fma_f32 v252, v13, v83, v14
	v_fma_f32 v248, v12, v78, v245
	v_fma_f32 v254, v12, v79, v251
	v_fma_f32 v249, 2.0, v244, v247
	v_fma_f32 v255, 2.0, v250, v253
	v_sub_f32_e32 v247, v247, v245
	v_sub_f32_e32 v253, v253, v251
	v_fma_f32 v246, -2.0, v244, v246
	v_fma_f32 v252, -2.0, v250, v252
	v_mul_f32_e32 v247, v247, v248
	v_mul_f32_e32 v253, v253, v254
	v_rcp_f32_e32 v247, v247
	v_rcp_f32_e32 v253, v253
	v_mul_f32_e32 v249, v249, v246
	v_mul_f32_e32 v255, v255, v252
	v_fma_f32 v20, v249, v247, v20
	v_fma_f32 v20, v255, v253, v20
	v_mul_f32_e32 v244, v84, v88
	v_mul_f32_e32 v250, v85, v89
	v_mul_f32_e64 v245, -v88, v88
	v_mul_f32_e64 v251, -v89, v89
	v_add_f32_e32 v246, v84, v88
	v_add_f32_e32 v252, v85, v89
	v_fma_f32 v245, -v84, v84, v245
	v_fma_f32 v251, -v85, v85, v251
	v_fma_f32 v247, v10, v246, v11
	v_fma_f32 v253, v10, v252, v11
	v_fma_f32 v246, v13, v96, v14
	v_fma_f32 v252, v13, v97, v14
	v_fma_f32 v248, v12, v92, v245
	v_fma_f32 v254, v12, v93, v251
	v_fma_f32 v249, 2.0, v244, v247
	v_fma_f32 v255, 2.0, v250, v253
	v_sub_f32_e32 v247, v247, v245
	v_sub_f32_e32 v253, v253, v251
	v_fma_f32 v246, -2.0, v244, v246
	v_fma_f32 v252, -2.0, v250, v252
	v_mul_f32_e32 v247, v247, v248
	v_mul_f32_e32 v253, v253, v254
	v_rcp_f32_e32 v247, v247
	v_rcp_f32_e32 v253, v253
	v_mul_f32_e32 v249, v249, v246
	v_mul_f32_e32 v255, v255, v252
	v_mul_f32_e32 v249, v249, v247
	v_mul_f32_e32 v255, v255, v253
	v_fma_f32 v19, v249, v15, v19
	v_fma_f32 v19, v255, v16, v19
	v_mul_f32_e32 v244, v86, v90
	v_mul_f32_e32 v250, v87, v91
	v_mul_f32_e64 v245, -v90, v90
	v_mul_f32_e64 v251, -v91, v91
	v_add_f32_e32 v246, v86, v90
	v_add_f32_e32 v252, v87, v91
	v_fma_f32 v245, -v86, v86, v245
	v_fma_f32 v251, -v87, v87, v251
	v_fma_f32 v247, v10, v246, v11
	v_fma_f32 v253, v10, v252, v11
	v_fma_f32 v246, v13, v98, v14
	v_fma_f32 v252, v13, v99, v14
	v_fma_f32 v248, v12, v94, v245
	v_fma_f32 v254, v12, v95, v251
	v_fma_f32 v249, 2.0, v244, v247
	v_fma_f32 v255, 2.0, v250, v253
	v_sub_f32_e32 v247, v247, v245
	v_sub_f32_e32 v253, v253, v251
	v_fma_f32 v246, -2.0, v244, v246
	v_fma_f32 v252, -2.0, v250, v252
	v_mul_f32_e32 v247, v247, v248
	v_mul_f32_e32 v253, v253, v254
	v_rcp_f32_e32 v247, v247
	v_rcp_f32_e32 v253, v253
	v_mul_f32_e32 v249, v249, v246
	v_mul_f32_e32 v255, v255, v252
	v_mul_f32_e32 v249, v249, v247
	v_mul_f32_e32 v255, v255, v253
	v_fma_f32 v20, v249, v17, v20
	v_fma_f32 v20, v255, v18, v20
	s_waitcnt vmcnt(12)
	v_cvt_pk_f16_f32 v36, v100, v104
	v_cvt_pk_f16_f32 v52, v132, v136
	v_pk_add_f16 v36, v36, -0.5 op_sel_hi:[1,0]
	v_pk_add_f16 v52, v52, -0.5 op_sel_hi:[1,0]
	v_pk_mul_f16 v68, v52, v52
	v_pk_mul_f16 v84, v36, v52
	v_pk_fma_f16 v68, v36, v36, v68
	v_cvt_pk_f16_f32 v40, v101, v105
	v_cvt_pk_f16_f32 v56, v133, v137
	v_pk_add_f16 v40, v40, -0.5 op_sel_hi:[1,0]
	v_pk_add_f16 v56, v56, -0.5 op_sel_hi:[1,0]
	v_pk_mul_f16 v72, v56, v56
	v_pk_mul_f16 v88, v40, v56
	v_pk_fma_f16 v72, v40, v40, v72
	v_cvt_pk_f16_f32 v44, v102, v106
	v_cvt_pk_f16_f32 v60, v134, v138
	v_pk_add_f16 v44, v44, -0.5 op_sel_hi:[1,0]
	v_pk_add_f16 v60, v60, -0.5 op_sel_hi:[1,0]
	v_pk_mul_f16 v76, v60, v60
	v_pk_mul_f16 v92, v44, v60
	v_pk_fma_f16 v76, v44, v44, v76
	v_cvt_pk_f16_f32 v48, v103, v107
	v_cvt_pk_f16_f32 v64, v135, v139
	v_pk_add_f16 v48, v48, -0.5 op_sel_hi:[1,0]
	v_pk_add_f16 v64, v64, -0.5 op_sel_hi:[1,0]
	v_pk_mul_f16 v80, v64, v64
	v_pk_mul_f16 v96, v48, v64
	v_pk_fma_f16 v80, v48, v48, v80
	s_waitcnt vmcnt(8)
	v_cvt_pk_f16_f32 v37, v108, v112
	v_cvt_pk_f16_f32 v53, v140, v144
	v_pk_add_f16 v37, v37, -0.5 op_sel_hi:[1,0]
	v_pk_add_f16 v53, v53, -0.5 op_sel_hi:[1,0]
	v_pk_mul_f16 v69, v53, v53
	v_pk_mul_f16 v85, v37, v53
	v_pk_fma_f16 v69, v37, v37, v69
	v_cvt_pk_f16_f32 v41, v109, v113
	v_cvt_pk_f16_f32 v57, v141, v145
	v_pk_add_f16 v41, v41, -0.5 op_sel_hi:[1,0]
	v_pk_add_f16 v57, v57, -0.5 op_sel_hi:[1,0]
	v_pk_mul_f16 v73, v57, v57
	v_pk_mul_f16 v89, v41, v57
	v_pk_fma_f16 v73, v41, v41, v73
	v_cvt_pk_f16_f32 v45, v110, v114
	v_cvt_pk_f16_f32 v61, v142, v146
	v_pk_add_f16 v45, v45, -0.5 op_sel_hi:[1,0]
	v_pk_add_f16 v61, v61, -0.5 op_sel_hi:[1,0]
	v_pk_mul_f16 v77, v61, v61
	v_pk_mul_f16 v93, v45, v61
	v_pk_fma_f16 v77, v45, v45, v77
	v_cvt_pk_f16_f32 v49, v111, v115
	v_cvt_pk_f16_f32 v65, v143, v147
	v_pk_add_f16 v49, v49, -0.5 op_sel_hi:[1,0]
	v_pk_add_f16 v65, v65, -0.5 op_sel_hi:[1,0]
	v_pk_mul_f16 v81, v65, v65
	v_pk_mul_f16 v97, v49, v65
	v_pk_fma_f16 v81, v49, v49, v81
	s_waitcnt vmcnt(4)
	v_cvt_pk_f16_f32 v38, v116, v120
	v_cvt_pk_f16_f32 v54, v148, v152
	v_pk_add_f16 v38, v38, -0.5 op_sel_hi:[1,0]
	v_pk_add_f16 v54, v54, -0.5 op_sel_hi:[1,0]
	v_pk_mul_f16 v70, v54, v54
	v_pk_mul_f16 v86, v38, v54
	v_pk_fma_f16 v70, v38, v38, v70
	v_cvt_pk_f16_f32 v42, v117, v121
	v_cvt_pk_f16_f32 v58, v149, v153
	v_pk_add_f16 v42, v42, -0.5 op_sel_hi:[1,0]
	v_pk_add_f16 v58, v58, -0.5 op_sel_hi:[1,0]
	v_pk_mul_f16 v74, v58, v58
	v_pk_mul_f16 v90, v42, v58
	v_pk_fma_f16 v74, v42, v42, v74
	v_cvt_pk_f16_f32 v46, v118, v122
	v_cvt_pk_f16_f32 v62, v150, v154
	v_pk_add_f16 v46, v46, -0.5 op_sel_hi:[1,0]
	v_pk_add_f16 v62, v62, -0.5 op_sel_hi:[1,0]
	v_pk_mul_f16 v78, v62, v62
	v_pk_mul_f16 v94, v46, v62
	v_pk_fma_f16 v78, v46, v46, v78
	v_cvt_pk_f16_f32 v50, v119, v123
	v_cvt_pk_f16_f32 v66, v151, v155
	v_pk_add_f16 v50, v50, -0.5 op_sel_hi:[1,0]
	v_pk_add_f16 v66, v66, -0.5 op_sel_hi:[1,0]
	v_pk_mul_f16 v82, v66, v66
	v_pk_mul_f16 v98, v50, v66
	v_pk_fma_f16 v82, v50, v50, v82
	s_waitcnt vmcnt(0)
	v_cvt_pk_f16_f32 v39, v124, v128
	v_cvt_pk_f16_f32 v55, v156, v160
	v_pk_add_f16 v39, v39, -0.5 op_sel_hi:[1,0]
	v_pk_add_f16 v55, v55, -0.5 op_sel_hi:[1,0]
	v_pk_mul_f16 v71, v55, v55
	v_pk_mul_f16 v87, v39, v55
	v_pk_fma_f16 v71, v39, v39, v71
	v_cvt_pk_f16_f32 v43, v125, v129
	v_cvt_pk_f16_f32 v59, v157, v161
	v_pk_add_f16 v43, v43, -0.5 op_sel_hi:[1,0]
	v_pk_add_f16 v59, v59, -0.5 op_sel_hi:[1,0]
	v_pk_mul_f16 v75, v59, v59
	v_pk_mul_f16 v91, v43, v59
	v_pk_fma_f16 v75, v43, v43, v75
	v_cvt_pk_f16_f32 v47, v126, v130
	v_cvt_pk_f16_f32 v63, v158, v162
	v_pk_add_f16 v47, v47, -0.5 op_sel_hi:[1,0]
	v_pk_add_f16 v63, v63, -0.5 op_sel_hi:[1,0]
	v_pk_mul_f16 v79, v63, v63
	v_pk_mul_f16 v95, v47, v63
	v_pk_fma_f16 v79, v47, v47, v79
	v_cvt_pk_f16_f32 v51, v127, v131
	v_cvt_pk_f16_f32 v67, v159, v163
	v_pk_add_f16 v51, v51, -0.5 op_sel_hi:[1,0]
	v_pk_add_f16 v67, v67, -0.5 op_sel_hi:[1,0]
	v_pk_mul_f16 v83, v67, v67
	v_pk_mul_f16 v99, v51, v67
	v_pk_fma_f16 v83, v51, v51, v83
	v_mfma_f32_16x16x32_f16 v[132:135], v[164:167], v[28:31], 0
	v_mfma_f32_16x16x32_f16 v[136:139], v[168:171], v[28:31], 0
	v_mfma_f32_16x16x32_f16 v[140:143], v[172:175], v[28:31], 0
	v_mfma_f32_16x16x32_f16 v[144:147], v[176:179], v[28:31], 0
	v_mfma_f32_16x16x32_f16 v[132:135], v[36:39], v[32:35], v[132:135]
	v_mfma_f32_16x16x32_f16 v[136:139], v[40:43], v[32:35], v[136:139]
	v_mfma_f32_16x16x32_f16 v[140:143], v[44:47], v[32:35], v[140:143]
	v_mfma_f32_16x16x32_f16 v[144:147], v[48:51], v[32:35], v[144:147]
	v_mfma_f32_16x16x32_f16 v[148:151], v[180:183], v[28:31], 0
	v_mfma_f32_16x16x32_f16 v[152:155], v[184:187], v[28:31], 0
	v_mfma_f32_16x16x32_f16 v[156:159], v[188:191], v[28:31], 0
	v_mfma_f32_16x16x32_f16 v[160:163], v[192:195], v[28:31], 0
	v_mfma_f32_16x16x32_f16 v[148:151], v[52:55], v[32:35], v[148:151]
	v_mfma_f32_16x16x32_f16 v[152:155], v[56:59], v[32:35], v[152:155]
	v_mfma_f32_16x16x32_f16 v[156:159], v[60:63], v[32:35], v[156:159]
	v_mfma_f32_16x16x32_f16 v[160:163], v[64:67], v[32:35], v[160:163]
	v_cvt_pk_f16_f32 v100, v132, v136
	v_cvt_pk_f16_f32 v101, v140, v144
	v_cvt_pk_f16_f32 v102, v133, v137
	v_cvt_pk_f16_f32 v103, v141, v145
	v_cvt_pk_f16_f32 v104, v134, v138
	v_cvt_pk_f16_f32 v105, v142, v146
	v_cvt_pk_f16_f32 v106, v135, v139
	v_cvt_pk_f16_f32 v107, v143, v147
	v_mfma_f32_16x16x32_f16 v[132:135], v[196:199], v[28:31], 0
	v_mfma_f32_16x16x32_f16 v[136:139], v[200:203], v[28:31], 0
	v_mfma_f32_16x16x32_f16 v[140:143], v[204:207], v[28:31], 0
	v_mfma_f32_16x16x32_f16 v[144:147], v[208:211], v[28:31], 0
	v_mfma_f32_16x16x32_f16 v[132:135], v[68:71], v[32:35], v[132:135]
	v_mfma_f32_16x16x32_f16 v[136:139], v[72:75], v[32:35], v[136:139]
	v_mfma_f32_16x16x32_f16 v[140:143], v[76:79], v[32:35], v[140:143]
	v_mfma_f32_16x16x32_f16 v[144:147], v[80:83], v[32:35], v[144:147]
	v_cvt_pk_f16_f32 v108, v148, v152
	v_cvt_pk_f16_f32 v109, v156, v160
	v_cvt_pk_f16_f32 v110, v149, v153
	v_cvt_pk_f16_f32 v111, v157, v161
	v_cvt_pk_f16_f32 v112, v150, v154
	v_cvt_pk_f16_f32 v113, v158, v162
	v_cvt_pk_f16_f32 v114, v151, v155
	v_cvt_pk_f16_f32 v115, v159, v163
	v_mfma_f32_16x16x32_f16 v[148:151], v[212:215], v[28:31], 0
	v_mfma_f32_16x16x32_f16 v[152:155], v[216:219], v[28:31], 0
	v_mfma_f32_16x16x32_f16 v[156:159], v[220:223], v[28:31], 0
	v_mfma_f32_16x16x32_f16 v[160:163], v[224:227], v[28:31], 0
	v_mfma_f32_16x16x32_f16 v[148:151], v[84:87], v[32:35], v[148:151]
	v_mfma_f32_16x16x32_f16 v[152:155], v[88:91], v[32:35], v[152:155]
	v_mfma_f32_16x16x32_f16 v[156:159], v[92:95], v[32:35], v[156:159]
	v_mfma_f32_16x16x32_f16 v[160:163], v[96:99], v[32:35], v[160:163]
	v_cvt_pk_f16_f32 v116, v132, v136
	v_cvt_pk_f16_f32 v117, v140, v144
	v_cvt_pk_f16_f32 v118, v133, v137
	v_cvt_pk_f16_f32 v119, v141, v145
	v_cvt_pk_f16_f32 v120, v134, v138
	v_cvt_pk_f16_f32 v121, v142, v146
	v_cvt_pk_f16_f32 v122, v135, v139
	v_cvt_pk_f16_f32 v123, v143, v147
	v_cvt_pk_f16_f32 v124, v148, v152
	v_cvt_pk_f16_f32 v125, v156, v160
	v_cvt_pk_f16_f32 v126, v149, v153
	v_cvt_pk_f16_f32 v127, v157, v161
	v_cvt_pk_f16_f32 v128, v150, v154
	v_cvt_pk_f16_f32 v129, v158, v162
	v_cvt_pk_f16_f32 v130, v151, v155
	v_cvt_pk_f16_f32 v131, v159, v163
	global_load_dwordx4 v[164:167], v23, s[84:85] offset:0 sc1 nt
	global_load_dwordx4 v[168:171], v23, s[84:85] offset:2048 sc1 nt
	global_load_dwordx4 v[180:183], v23, s[88:89] offset:0 sc1 nt
	global_load_dwordx4 v[184:187], v23, s[88:89] offset:2048 sc1 nt
	global_load_dwordx4 v[172:175], v23, s[86:87] offset:0 sc1 nt
	global_load_dwordx4 v[176:179], v23, s[86:87] offset:2048 sc1 nt
	global_load_dwordx4 v[188:191], v23, s[90:91] offset:0 sc1 nt
	global_load_dwordx4 v[192:195], v23, s[90:91] offset:2048 sc1 nt
	s_mov_b64 exec, s[38:39]
	ds_write_b128 v4, v[104:107] offset:16384
	ds_write_b128 v4, v[112:115] offset:16896
	ds_write_b128 v4, v[120:123] offset:17408
	ds_write_b128 v4, v[128:131] offset:17920
	s_mov_b64 exec, -1
	v_mfma_f32_16x16x32_f16 v[132:135], v[24:27], v[100:103], 0
	v_mfma_f32_16x16x32_f16 v[136:139], v[24:27], v[108:111], 0
	v_mfma_f32_16x16x32_f16 v[140:143], v[24:27], v[116:119], v[0:3]
	v_mfma_f32_16x16x32_f16 v[144:147], v[24:27], v[124:127], 0
	v_mfma_f32_16x16x32_f16 v[148:151], v[28:31], v[100:103], 0
	v_mfma_f32_16x16x32_f16 v[152:155], v[28:31], v[108:111], 0
	v_mfma_f32_16x16x32_f16 v[156:159], v[28:31], v[116:119], v[0:3]
	v_mfma_f32_16x16x32_f16 v[160:163], v[28:31], v[124:127], 0
	v_mfma_f32_16x16x32_f16 v[148:151], v[32:35], v[104:107], v[148:151]
	v_mfma_f32_16x16x32_f16 v[152:155], v[32:35], v[112:115], v[152:155]
	v_mfma_f32_16x16x32_f16 v[156:159], v[32:35], v[120:123], v[156:159]
	v_mfma_f32_16x16x32_f16 v[160:163], v[32:35], v[128:131], v[160:163]
	s_waitcnt lgkmcnt(0)
	ds_write_b32 v6, v6 offset:32
	ds_read_b32 v9, v7 offset:32
	v_mul_f32_e32 v244, v132, v136
	v_mul_f32_e32 v250, v133, v137
	v_mul_f32_e64 v245, -v136, v136
	v_mul_f32_e64 v251, -v137, v137
	v_add_f32_e32 v246, v132, v136
	v_add_f32_e32 v252, v133, v137
	v_fma_f32 v245, -v132, v132, v245
	v_fma_f32 v251, -v133, v133, v251
	v_fma_f32 v247, v10, v246, v11
	v_fma_f32 v253, v10, v252, v11
	v_fma_f32 v246, v13, v144, v14
	v_fma_f32 v252, v13, v145, v14
	v_fma_f32 v248, v12, v140, v245
	v_fma_f32 v254, v12, v141, v251
	v_fma_f32 v249, 2.0, v244, v247
	v_fma_f32 v255, 2.0, v250, v253
	v_sub_f32_e32 v247, v247, v245
	v_sub_f32_e32 v253, v253, v251
	v_fma_f32 v246, -2.0, v244, v246
	v_fma_f32 v252, -2.0, v250, v252
	v_mul_f32_e32 v247, v247, v248
	v_mul_f32_e32 v253, v253, v254
	v_rcp_f32_e32 v247, v247
	v_rcp_f32_e32 v253, v253
	v_mul_f32_e32 v249, v249, v246
	v_mul_f32_e32 v255, v255, v252
	v_fma_f32 v19, v249, v247, v19
	v_fma_f32 v19, v255, v253, v19
	v_mul_f32_e32 v244, v134, v138
	v_mul_f32_e32 v250, v135, v139
	v_mul_f32_e64 v245, -v138, v138
	v_mul_f32_e64 v251, -v139, v139
	v_add_f32_e32 v246, v134, v138
	v_add_f32_e32 v252, v135, v139
	v_fma_f32 v245, -v134, v134, v245
	v_fma_f32 v251, -v135, v135, v251
	v_fma_f32 v247, v10, v246, v11
	v_fma_f32 v253, v10, v252, v11
	v_fma_f32 v246, v13, v146, v14
	v_fma_f32 v252, v13, v147, v14
	v_fma_f32 v248, v12, v142, v245
	v_fma_f32 v254, v12, v143, v251
	v_fma_f32 v249, 2.0, v244, v247
	v_fma_f32 v255, 2.0, v250, v253
	v_sub_f32_e32 v247, v247, v245
	v_sub_f32_e32 v253, v253, v251
	v_fma_f32 v246, -2.0, v244, v246
	v_fma_f32 v252, -2.0, v250, v252
	v_mul_f32_e32 v247, v247, v248
	v_mul_f32_e32 v253, v253, v254
	v_rcp_f32_e32 v247, v247
	v_rcp_f32_e32 v253, v253
	v_mul_f32_e32 v249, v249, v246
	v_mul_f32_e32 v255, v255, v252
	v_fma_f32 v20, v249, v247, v20
	v_fma_f32 v20, v255, v253, v20
	v_mfma_f32_16x16x32_f16 v[132:135], v[24:27], v[104:107], 0
	v_mfma_f32_16x16x32_f16 v[136:139], v[24:27], v[112:115], 0
	v_mfma_f32_16x16x32_f16 v[140:143], v[24:27], v[120:123], v[0:3]
	v_mfma_f32_16x16x32_f16 v[144:147], v[24:27], v[128:131], 0
	s_waitcnt lgkmcnt(0)
	v_cmp_ne_u32_e32 vcc, 0, v9
	s_cbranch_vccnz .Lq_go_1
